# v24 + P.V pass of both diff-attention loops fetches V fragment groups two MFMA groups ahead (3 slots, lgkmcnt(8)) instead of one
# speedup vs baseline: 1.0240x; 1.0069x over previous
.LBB0_188:
	s_waitcnt lgkmcnt(0)
	v_add_u32_e32 v0, s44, v224
	ds_read_b64_tr_b16 v[160:161], v0 offset:0
	ds_read_b64_tr_b16 v[162:163], v0 offset:0x800
	ds_read_b64_tr_b16 v[164:165], v0 offset:0x200
	ds_read_b64_tr_b16 v[166:167], v0 offset:0xa00
	ds_read_b64_tr_b16 v[168:169], v0 offset:0x400
	ds_read_b64_tr_b16 v[170:171], v0 offset:0xc00
	ds_read_b64_tr_b16 v[172:173], v0 offset:0x600
	ds_read_b64_tr_b16 v[174:175], v0 offset:0xe00
	ds_read_b64_tr_b16 v[244:245], v0 offset:0x1000
	ds_read_b64_tr_b16 v[246:247], v0 offset:0x1800
	ds_read_b64_tr_b16 v[248:249], v0 offset:0x1200
	ds_read_b64_tr_b16 v[250:251], v0 offset:0x1a00
	s_waitcnt lgkmcnt(8)
	s_nop 0
	v_mfma_f32_32x32x16_bf16 v[112:127], v[208:211], v[160:163], v[112:127]
	v_mfma_f32_32x32x16_bf16 v[96:111], v[208:211], v[164:167], v[96:111]
	v_mfma_f32_32x32x16_bf16 v[128:143], v[156:159], v[160:163], v[128:143]
	v_mfma_f32_32x32x16_bf16 v[80:95], v[156:159], v[164:167], v[80:95]
	ds_read_b64_tr_b16 v[160:161], v0 offset:0x1400
	ds_read_b64_tr_b16 v[162:163], v0 offset:0x1c00
	ds_read_b64_tr_b16 v[164:165], v0 offset:0x1600
	ds_read_b64_tr_b16 v[166:167], v0 offset:0x1e00
	s_waitcnt lgkmcnt(8)
	v_mfma_f32_32x32x16_bf16 v[64:79], v[208:211], v[168:171], v[64:79]
	v_mfma_f32_32x32x16_bf16 v[48:63], v[208:211], v[172:175], v[48:63]
	v_mfma_f32_32x32x16_bf16 v[32:47], v[156:159], v[168:171], v[32:47]
	v_mfma_f32_32x32x16_bf16 v[16:31], v[156:159], v[172:175], v[16:31]
	ds_read_b64_tr_b16 v[168:169], v0 offset:0x2000
	ds_read_b64_tr_b16 v[170:171], v0 offset:0x2800
	ds_read_b64_tr_b16 v[172:173], v0 offset:0x2200
	ds_read_b64_tr_b16 v[174:175], v0 offset:0x2a00
	s_waitcnt lgkmcnt(8)
	v_mfma_f32_32x32x16_bf16 v[112:127], v[10:13], v[244:247], v[112:127]
	v_mfma_f32_32x32x16_bf16 v[96:111], v[10:13], v[248:251], v[96:111]
	v_mfma_f32_32x32x16_bf16 v[128:143], v[152:155], v[244:247], v[128:143]
	v_mfma_f32_32x32x16_bf16 v[80:95], v[152:155], v[248:251], v[80:95]
	ds_read_b64_tr_b16 v[244:245], v0 offset:0x2400
	ds_read_b64_tr_b16 v[246:247], v0 offset:0x2c00
	ds_read_b64_tr_b16 v[248:249], v0 offset:0x2600
	ds_read_b64_tr_b16 v[250:251], v0 offset:0x2e00
	s_waitcnt lgkmcnt(8)
	v_mfma_f32_32x32x16_bf16 v[64:79], v[10:13], v[160:163], v[64:79]
	v_mfma_f32_32x32x16_bf16 v[48:63], v[10:13], v[164:167], v[48:63]
	v_mfma_f32_32x32x16_bf16 v[32:47], v[152:155], v[160:163], v[32:47]
	v_mfma_f32_32x32x16_bf16 v[16:31], v[152:155], v[164:167], v[16:31]
	ds_read_b64_tr_b16 v[160:161], v0 offset:0x3000
	ds_read_b64_tr_b16 v[162:163], v0 offset:0x3800
	ds_read_b64_tr_b16 v[164:165], v0 offset:0x3200
	ds_read_b64_tr_b16 v[166:167], v0 offset:0x3a00
	s_waitcnt lgkmcnt(8)
	v_mfma_f32_32x32x16_bf16 v[112:127], v[6:9], v[168:171], v[112:127]
	v_mfma_f32_32x32x16_bf16 v[96:111], v[6:9], v[172:175], v[96:111]
	v_mfma_f32_32x32x16_bf16 v[128:143], v[148:151], v[168:171], v[128:143]
	v_mfma_f32_32x32x16_bf16 v[80:95], v[148:151], v[172:175], v[80:95]
	ds_read_b64_tr_b16 v[168:169], v0 offset:0x3400
	ds_read_b64_tr_b16 v[170:171], v0 offset:0x3c00
	ds_read_b64_tr_b16 v[172:173], v0 offset:0x3600
	ds_read_b64_tr_b16 v[174:175], v0 offset:0x3e00
	s_waitcnt lgkmcnt(8)
	v_mfma_f32_32x32x16_bf16 v[64:79], v[6:9], v[244:247], v[64:79]
	v_mfma_f32_32x32x16_bf16 v[48:63], v[6:9], v[248:251], v[48:63]
	v_mfma_f32_32x32x16_bf16 v[32:47], v[148:151], v[244:247], v[32:47]
	v_mfma_f32_32x32x16_bf16 v[16:31], v[148:151], v[248:251], v[16:31]
	s_waitcnt lgkmcnt(4)
	v_mfma_f32_32x32x16_bf16 v[112:127], v[2:5], v[160:163], v[112:127]
	v_mfma_f32_32x32x16_bf16 v[96:111], v[2:5], v[164:167], v[96:111]
	v_mfma_f32_32x32x16_bf16 v[128:143], v[144:147], v[160:163], v[128:143]
	v_mfma_f32_32x32x16_bf16 v[80:95], v[144:147], v[164:167], v[80:95]
	s_waitcnt lgkmcnt(0)
	v_mfma_f32_32x32x16_bf16 v[64:79], v[2:5], v[168:171], v[64:79]
	v_mfma_f32_32x32x16_bf16 v[48:63], v[2:5], v[172:175], v[48:63]
	v_mfma_f32_32x32x16_bf16 v[32:47], v[144:147], v[168:171], v[32:47]
	v_mfma_f32_32x32x16_bf16 v[16:31], v[144:147], v[172:175], v[16:31]

.LBB0_205:
	v_add_u32_e32 v219, v212, v232
	v_add_u32_e32 v212, v212, v233
	s_waitcnt lgkmcnt(0)
	v_mfma_f32_32x32x16_bf16 v[144:159], v[248:251], v[192:195], v[144:159]
	ds_read_b128 v[248:251], v219
	v_mfma_f32_32x32x16_bf16 v[160:175], v[236:239], v[192:195], v[160:175]
	ds_read_b128 v[236:239], v219 offset:8192
	v_mfma_f32_32x32x16_bf16 v[144:159], v[240:243], v[196:199], v[144:159]
	ds_read_b128 v[240:243], v212
	v_mfma_f32_32x32x16_bf16 v[160:175], v[244:247], v[196:199], v[160:175]
	ds_read_b128 v[244:247], v212 offset:8192
	s_waitcnt lgkmcnt(3)
	v_mfma_f32_32x32x16_bf16 v[144:159], v[248:251], v[200:203], v[144:159]
	s_waitcnt lgkmcnt(2)
	v_mfma_f32_32x32x16_bf16 v[160:175], v[236:239], v[200:203], v[160:175]
	v_add_f32_e32 v212, v213, v218
	v_add_f32_e32 v235, v235, v212
	s_waitcnt lgkmcnt(1)
	v_mfma_f32_32x32x16_bf16 v[144:159], v[240:243], v[204:207], v[144:159]
	s_waitcnt lgkmcnt(0)
	v_mfma_f32_32x32x16_bf16 v[160:175], v[244:247], v[204:207], v[160:175]
	s_nop 10
	v_exp_f32_e32 v212, v144
	v_exp_f32_e32 v218, v145
	v_exp_f32_e32 v242, v148
	v_exp_f32_e32 v244, v149
	v_exp_f32_e32 v213, v152
	v_exp_f32_e32 v219, v153
	v_exp_f32_e32 v243, v156
	v_exp_f32_e32 v245, v157
	v_exp_f32_e32 v236, v146
	v_exp_f32_e32 v150, v150
	v_exp_f32_e32 v248, v151
	v_exp_f32_e32 v237, v154
	v_exp_f32_e32 v151, v158
	v_exp_f32_e32 v238, v147
	v_exp_f32_e32 v239, v155
	v_exp_f32_e32 v249, v159
	v_exp_f32_e32 v160, v160
	v_exp_f32_e32 v220, v161
	v_exp_f32_e32 v164, v164
	v_exp_f32_e32 v246, v165
	v_exp_f32_e32 v161, v168
	v_exp_f32_e32 v165, v172
	v_exp_f32_e32 v221, v169
	v_exp_f32_e32 v247, v173
	v_pk_add_f32 v[144:145], v[212:213], v[218:219]
	v_pk_add_f32 v[146:147], v[242:243], v[244:245]
	v_exp_f32_e32 v162, v162
	v_exp_f32_e32 v240, v163
	v_exp_f32_e32 v166, v166
	v_exp_f32_e32 v250, v167
	v_exp_f32_e32 v163, v170
	v_exp_f32_e32 v167, v174
	v_pk_add_f32 v[144:145], v[236:237], v[144:145]
	v_pk_add_f32 v[146:147], v[150:151], v[146:147]
	v_exp_f32_e32 v241, v171
	v_exp_f32_e32 v251, v175
	v_pk_add_f32 v[144:145], v[238:239], v[144:145]
	v_pk_add_f32 v[146:147], v[248:249], v[146:147]
	v_pk_add_f32 v[144:145], v[160:161], v[144:145]
	v_pk_add_f32 v[146:147], v[164:165], v[146:147]
	v_pk_add_f32 v[144:145], v[220:221], v[144:145]
	v_pk_add_f32 v[146:147], v[246:247], v[146:147]
	v_pk_add_f32 v[144:145], v[162:163], v[144:145]
	v_pk_add_f32 v[146:147], v[166:167], v[146:147]
	v_pk_add_f32 v[144:145], v[240:241], v[144:145]
	v_pk_add_f32 v[146:147], v[250:251], v[146:147]
	v_cvt_pk_bf16_f32 v148, v213, v219
	v_pk_add_f32 v[144:145], v[144:145], v[146:147]
	v_cvt_pk_bf16_f32 v146, v242, v244
	v_pk_add_f32 v[144:145], v[144:145], v[144:145] op_sel:[0,1] op_sel_hi:[1,0]
	v_cvt_pk_bf16_f32 v147, v150, v248
	v_mov_b32_e32 v145, v144
	s_nop 1
	v_permlane32_swap_b32_e32 v144, v145
	v_add_f32_e32 v144, v144, v145
	v_add_f32_e32 v234, v234, v144
	v_cvt_pk_bf16_f32 v144, v212, v218
	v_cvt_pk_bf16_f32 v145, v236, v238
	v_cvt_pk_bf16_f32 v149, v237, v239
	v_cvt_pk_bf16_f32 v150, v243, v245
	v_cvt_pk_bf16_f32 v151, v151, v249
	v_cvt_pk_bf16_f32 v152, v160, v220
	v_cvt_pk_bf16_f32 v153, v162, v240
	v_cvt_pk_bf16_f32 v154, v164, v246
	v_cvt_pk_bf16_f32 v155, v166, v250
	v_cvt_pk_bf16_f32 v156, v161, v221
	v_cvt_pk_bf16_f32 v157, v163, v241
	v_cvt_pk_bf16_f32 v158, v165, v247
	v_cvt_pk_bf16_f32 v159, v167, v251
	v_permlane32_swap_b32_e32 v144, v146
	v_permlane32_swap_b32_e32 v145, v147
	v_permlane32_swap_b32_e32 v148, v150
	v_permlane32_swap_b32_e32 v149, v151
	v_permlane32_swap_b32_e32 v152, v154
	v_permlane32_swap_b32_e32 v153, v155
	v_permlane32_swap_b32_e32 v156, v158
	v_permlane32_swap_b32_e32 v157, v159
	s_waitcnt lgkmcnt(0)
	v_add_u32_e32 v212, s56, v224
	ds_read_b64_tr_b16 v[160:161], v212 offset:0
	ds_read_b64_tr_b16 v[162:163], v212 offset:0x800
	ds_read_b64_tr_b16 v[164:165], v212 offset:0x200
	ds_read_b64_tr_b16 v[166:167], v212 offset:0xa00
	ds_read_b64_tr_b16 v[168:169], v212 offset:0x400
	ds_read_b64_tr_b16 v[170:171], v212 offset:0xc00
	ds_read_b64_tr_b16 v[172:173], v212 offset:0x600
	ds_read_b64_tr_b16 v[174:175], v212 offset:0xe00
	ds_read_b64_tr_b16 v[244:245], v212 offset:0x1000
	ds_read_b64_tr_b16 v[246:247], v212 offset:0x1800
	ds_read_b64_tr_b16 v[248:249], v212 offset:0x1200
	ds_read_b64_tr_b16 v[250:251], v212 offset:0x1a00
	s_waitcnt lgkmcnt(8)
	s_nop 0
	v_mfma_f32_32x32x16_bf16 v[112:127], v[208:211], v[160:163], v[112:127]
	v_mfma_f32_32x32x16_bf16 v[96:111], v[208:211], v[164:167], v[96:111]
	v_mfma_f32_32x32x16_bf16 v[128:143], v[144:147], v[160:163], v[128:143]
	v_mfma_f32_32x32x16_bf16 v[80:95], v[144:147], v[164:167], v[80:95]
	ds_read_b64_tr_b16 v[160:161], v212 offset:0x1400
	ds_read_b64_tr_b16 v[162:163], v212 offset:0x1c00
	ds_read_b64_tr_b16 v[164:165], v212 offset:0x1600
	ds_read_b64_tr_b16 v[166:167], v212 offset:0x1e00
	s_waitcnt lgkmcnt(8)
	v_mfma_f32_32x32x16_bf16 v[64:79], v[208:211], v[168:171], v[64:79]
	v_mfma_f32_32x32x16_bf16 v[48:63], v[208:211], v[172:175], v[48:63]
	v_mfma_f32_32x32x16_bf16 v[32:47], v[144:147], v[168:171], v[32:47]
	v_mfma_f32_32x32x16_bf16 v[16:31], v[144:147], v[172:175], v[16:31]
	ds_read_b64_tr_b16 v[168:169], v212 offset:0x2000
	ds_read_b64_tr_b16 v[170:171], v212 offset:0x2800
	ds_read_b64_tr_b16 v[172:173], v212 offset:0x2200
	ds_read_b64_tr_b16 v[174:175], v212 offset:0x2a00
	s_waitcnt lgkmcnt(8)
	v_mfma_f32_32x32x16_bf16 v[112:127], v[10:13], v[244:247], v[112:127]
	v_mfma_f32_32x32x16_bf16 v[96:111], v[10:13], v[248:251], v[96:111]
	v_mfma_f32_32x32x16_bf16 v[128:143], v[148:151], v[244:247], v[128:143]
	v_mfma_f32_32x32x16_bf16 v[80:95], v[148:151], v[248:251], v[80:95]
	ds_read_b64_tr_b16 v[244:245], v212 offset:0x2400
	ds_read_b64_tr_b16 v[246:247], v212 offset:0x2c00
	ds_read_b64_tr_b16 v[248:249], v212 offset:0x2600
	ds_read_b64_tr_b16 v[250:251], v212 offset:0x2e00
	s_waitcnt lgkmcnt(8)
	v_mfma_f32_32x32x16_bf16 v[64:79], v[10:13], v[160:163], v[64:79]
	v_mfma_f32_32x32x16_bf16 v[48:63], v[10:13], v[164:167], v[48:63]
	v_mfma_f32_32x32x16_bf16 v[32:47], v[148:151], v[160:163], v[32:47]
	v_mfma_f32_32x32x16_bf16 v[16:31], v[148:151], v[164:167], v[16:31]
	ds_read_b64_tr_b16 v[160:161], v212 offset:0x3000
	ds_read_b64_tr_b16 v[162:163], v212 offset:0x3800
	ds_read_b64_tr_b16 v[164:165], v212 offset:0x3200
	ds_read_b64_tr_b16 v[166:167], v212 offset:0x3a00
	s_waitcnt lgkmcnt(8)
	v_mfma_f32_32x32x16_bf16 v[112:127], v[6:9], v[168:171], v[112:127]
	v_mfma_f32_32x32x16_bf16 v[96:111], v[6:9], v[172:175], v[96:111]
	v_mfma_f32_32x32x16_bf16 v[128:143], v[152:155], v[168:171], v[128:143]
	v_mfma_f32_32x32x16_bf16 v[80:95], v[152:155], v[172:175], v[80:95]
	ds_read_b64_tr_b16 v[168:169], v212 offset:0x3400
	ds_read_b64_tr_b16 v[170:171], v212 offset:0x3c00
	ds_read_b64_tr_b16 v[172:173], v212 offset:0x3600
	ds_read_b64_tr_b16 v[174:175], v212 offset:0x3e00
	s_waitcnt lgkmcnt(8)
	v_mfma_f32_32x32x16_bf16 v[64:79], v[6:9], v[244:247], v[64:79]
	v_mfma_f32_32x32x16_bf16 v[48:63], v[6:9], v[248:251], v[48:63]
	v_mfma_f32_32x32x16_bf16 v[32:47], v[152:155], v[244:247], v[32:47]
	v_mfma_f32_32x32x16_bf16 v[16:31], v[152:155], v[248:251], v[16:31]
	s_waitcnt lgkmcnt(4)
	v_mfma_f32_32x32x16_bf16 v[112:127], v[2:5], v[160:163], v[112:127]
	v_mfma_f32_32x32x16_bf16 v[96:111], v[2:5], v[164:167], v[96:111]
	v_mfma_f32_32x32x16_bf16 v[128:143], v[156:159], v[160:163], v[128:143]
	v_mfma_f32_32x32x16_bf16 v[80:95], v[156:159], v[164:167], v[80:95]
	s_waitcnt lgkmcnt(0)
	v_mfma_f32_32x32x16_bf16 v[64:79], v[2:5], v[168:171], v[64:79]
	v_mfma_f32_32x32x16_bf16 v[48:63], v[2:5], v[172:175], v[48:63]
	v_mfma_f32_32x32x16_bf16 v[32:47], v[156:159], v[168:171], v[32:47]
	v_mfma_f32_32x32x16_bf16 v[16:31], v[156:159], v[172:175], v[16:31]
	s_add_i32 s42, s56, 0x4000
	s_cmpk_lg_u32 s56, 0xc000
	s_cselect_b32 s56, s42, 0
	s_add_i32 s42, s90, 0x4000
	s_cmpk_lg_u32 s90, 0xc000
	s_cselect_b32 s90, s42, 0
	s_add_u32 s40, s40, 0x60000
	s_addc_u32 s41, s41, 0
	s_addk_i32 s73, 0x100
	s_add_i32 s72, s72, 64
	s_add_i32 s71, s71, 1
	s_cmpk_eq_i32 s73, 0x4000
	s_cbranch_scc1 .LBB0_220
